# v84 + P11 ranking of the 50 candidate sums per token by 16-key sorts and bitonic top-16 merges (785 instructions instead of 1516); the interleaved row-scale work keeps its order
# speedup vs baseline: 1.0063x; 1.0063x over previous
; #define LAS __attribute__((address_space(3)))
; #define INS16(A_, X_) do { float x_ = (X_); _Pragma("unroll") for (int i_ = 0; i_ < 16; ++i_) { const float hi_ = fmaxf(A_[i_], x_); x_ = fminf(A_[i_], x_); A_[i_] = hi_; } } while (0)
; __device__ __forceinline__ float uniq_key(float s, int n) { return __uint_as_float((__float_as_uint(s) & ~0xffu) | (unsigned)(255 - n)); }
; __device__ __forceinline__ void p11_route(Frame& F) {
;     ...
;         if (F.lane < 16) {
;             const LAS float* r0 = sc + F.lane * 129; const LAS float* r1 = sc + (16 + F.lane) * 129;
;             float v0[16], v1[16];
; #pragma unroll
;             for (int i = 0; i < 16; ++i) { v0[i] = r0[i]; v1[i] = r1[i]; }
;             float b[16];
; #pragma unroll
;             for (int i = 0; i < 16; ++i) b[i] = -INFINITY;
;             { int p = 0;
; #pragma unroll
;               for (int i = 0; i < 16; ++i)
; #pragma unroll
;                   for (int j = 0; j < 16; ++j) if ((i + 1) * (j + 1) <= 16) { INS16(b, uniq_key(v0[i] + v1[j], p)); ++p; } }
.LBB0_3219:
	s_waitcnt lgkmcnt(0)
	v_add_u32_e32 v188, 0x2040, v154
	ds_read2_b32 v[126:127], v154 offset0:0 offset1:1
	ds_read2_b32 v[128:129], v154 offset0:2 offset1:3
	ds_read2_b32 v[130:131], v154 offset0:4 offset1:5
	ds_read2_b32 v[132:133], v154 offset0:6 offset1:7
	ds_read2_b32 v[134:135], v154 offset0:8 offset1:9
	ds_read2_b32 v[136:137], v154 offset0:10 offset1:11
	ds_read2_b32 v[138:139], v154 offset0:12 offset1:13
	ds_read2_b32 v[140:141], v154 offset0:14 offset1:15
	ds_read2_b32 v[142:143], v188 offset0:0 offset1:1
	ds_read2_b32 v[144:145], v188 offset0:2 offset1:3
	ds_read2_b32 v[160:161], v188 offset0:4 offset1:5
	ds_read2_b32 v[162:163], v188 offset0:6 offset1:7
	ds_read2_b32 v[164:165], v188 offset0:8 offset1:9
	ds_read2_b32 v[166:167], v188 offset0:10 offset1:11
	ds_read2_b32 v[168:169], v188 offset0:12 offset1:13
	ds_read2_b32 v[170:171], v188 offset0:14 offset1:15
	s_waitcnt lgkmcnt(0)
	v_add_f32_e32 v222, v126, v142
	v_and_b32_e32 v222, 0xffffff00, v222
	v_or_b32_e32 v222, 0xff, v222
	v_add_f32_e32 v223, v126, v143
	v_and_b32_e32 v223, 0xffffff00, v223
	v_or_b32_e32 v223, 0xfe, v223
	v_add_f32_e32 v224, v126, v144
	v_and_b32_e32 v224, 0xffffff00, v224
	v_or_b32_e32 v224, 0xfd, v224
	v_add_f32_e32 v225, v126, v145
	v_and_b32_e32 v225, 0xffffff00, v225
	v_or_b32_e32 v225, 0xfc, v225
	v_add_f32_e32 v226, v126, v160
	v_and_b32_e32 v226, 0xffffff00, v226
	v_or_b32_e32 v226, 0xfb, v226
	v_add_f32_e32 v227, v126, v161
	v_and_b32_e32 v227, 0xffffff00, v227
	v_or_b32_e32 v227, 0xfa, v227
	v_add_f32_e32 v228, v126, v162
	v_and_b32_e32 v228, 0xffffff00, v228
	v_or_b32_e32 v228, 0xf9, v228
	v_add_f32_e32 v229, v126, v163
	v_and_b32_e32 v229, 0xffffff00, v229
	v_or_b32_e32 v229, 0xf8, v229
	v_add_f32_e32 v230, v126, v164
	v_and_b32_e32 v230, 0xffffff00, v230
	v_or_b32_e32 v230, 0xf7, v230
	v_add_f32_e32 v231, v126, v165
	v_and_b32_e32 v231, 0xffffff00, v231
	v_or_b32_e32 v231, 0xf6, v231
	v_add_f32_e32 v232, v126, v166
	v_and_b32_e32 v232, 0xffffff00, v232
	v_or_b32_e32 v232, 0xf5, v232
	v_add_f32_e32 v233, v126, v167
	v_and_b32_e32 v233, 0xffffff00, v233
	v_or_b32_e32 v233, 0xf4, v233
	v_add_f32_e32 v234, v126, v168
	v_and_b32_e32 v234, 0xffffff00, v234
	v_or_b32_e32 v234, 0xf3, v234
	v_add_f32_e32 v235, v126, v169
	v_and_b32_e32 v235, 0xffffff00, v235
	v_or_b32_e32 v235, 0xf2, v235
	v_add_f32_e32 v236, v126, v170
	v_and_b32_e32 v236, 0xffffff00, v236
	v_or_b32_e32 v236, 0xf1, v236
	v_add_f32_e32 v237, v126, v171
	v_and_b32_e32 v237, 0xffffff00, v237
	v_or_b32_e32 v237, 0xf0, v237
	v_max_f32_e32 v254, v222, v223
	v_min_f32_e32 v223, v222, v223
	v_max_f32_e32 v222, v224, v225
	v_min_f32_e32 v225, v224, v225
	v_max_f32_e32 v224, v254, v222
	v_min_f32_e32 v222, v254, v222
	v_max_f32_e32 v254, v223, v225
	v_min_f32_e32 v225, v223, v225
	v_max_f32_e32 v223, v254, v222
	v_min_f32_e32 v222, v254, v222
	v_max_f32_e32 v254, v226, v227
	v_min_f32_e32 v227, v226, v227
	v_max_f32_e32 v226, v228, v229
	v_min_f32_e32 v229, v228, v229
	v_max_f32_e32 v228, v254, v226
	v_min_f32_e32 v226, v254, v226
	v_max_f32_e32 v254, v227, v229
	v_min_f32_e32 v229, v227, v229
	v_max_f32_e32 v227, v254, v226
	v_min_f32_e32 v226, v254, v226
	v_max_f32_e32 v254, v224, v228
	v_min_f32_e32 v228, v224, v228
	v_max_f32_e32 v224, v222, v226
	v_min_f32_e32 v226, v222, v226
	v_max_f32_e32 v222, v224, v228
	v_min_f32_e32 v228, v224, v228
	v_max_f32_e32 v224, v223, v227
	v_min_f32_e32 v227, v223, v227
	v_max_f32_e32 v223, v225, v229
	v_min_f32_e32 v229, v225, v229
	v_max_f32_e32 v225, v223, v227
	v_min_f32_e32 v227, v223, v227
	v_max_f32_e32 v223, v224, v222
	v_min_f32_e32 v222, v224, v222
	v_max_f32_e32 v224, v225, v228
	v_min_f32_e32 v228, v225, v228
	v_max_f32_e32 v225, v227, v226
	v_min_f32_e32 v226, v227, v226
	v_max_f32_e32 v227, v230, v231
	v_min_f32_e32 v231, v230, v231
	v_max_f32_e32 v230, v232, v233
	v_min_f32_e32 v233, v232, v233
	v_max_f32_e32 v232, v227, v230
	v_min_f32_e32 v230, v227, v230
	v_max_f32_e32 v227, v231, v233
	v_min_f32_e32 v233, v231, v233
	v_max_f32_e32 v231, v227, v230
	v_min_f32_e32 v230, v227, v230
	v_max_f32_e32 v227, v234, v235
	v_min_f32_e32 v235, v234, v235
	v_max_f32_e32 v234, v236, v237
	v_min_f32_e32 v237, v236, v237
	v_max_f32_e32 v236, v227, v234
	v_min_f32_e32 v234, v227, v234
	v_max_f32_e32 v227, v235, v237
	v_min_f32_e32 v237, v235, v237
	v_max_f32_e32 v235, v227, v234
	v_min_f32_e32 v234, v227, v234
	v_max_f32_e32 v227, v232, v236
	v_min_f32_e32 v236, v232, v236
	v_max_f32_e32 v232, v230, v234
	v_min_f32_e32 v234, v230, v234
	v_max_f32_e32 v230, v232, v236
	v_min_f32_e32 v236, v232, v236
	v_max_f32_e32 v232, v231, v235
	v_min_f32_e32 v235, v231, v235
	v_max_f32_e32 v231, v233, v237
	v_min_f32_e32 v237, v233, v237
	v_max_f32_e32 v233, v231, v235
	v_min_f32_e32 v235, v231, v235
	v_max_f32_e32 v231, v232, v230
	v_min_f32_e32 v230, v232, v230
	v_max_f32_e32 v232, v233, v236
	v_min_f32_e32 v236, v233, v236
	v_max_f32_e32 v233, v235, v234
	v_min_f32_e32 v234, v235, v234
	v_max_f32_e32 v235, v254, v227
	v_min_f32_e32 v227, v254, v227
	v_max_f32_e32 v254, v228, v236
	v_min_f32_e32 v236, v228, v236
	v_max_f32_e32 v228, v254, v227
	v_min_f32_e32 v227, v254, v227
	v_max_f32_e32 v254, v222, v230
	v_min_f32_e32 v230, v222, v230
	v_max_f32_e32 v222, v226, v234
	v_min_f32_e32 v234, v226, v234
	v_max_f32_e32 v226, v222, v230
	v_min_f32_e32 v230, v222, v230
	v_max_f32_e32 v222, v254, v228
	v_min_f32_e32 v228, v254, v228
	v_max_f32_e32 v254, v226, v227
	v_min_f32_e32 v227, v226, v227
	v_max_f32_e32 v226, v230, v236
	v_min_f32_e32 v236, v230, v236
	v_max_f32_e32 v230, v223, v231
	v_min_f32_e32 v231, v223, v231
	v_max_f32_e32 v223, v225, v233
; #define INS16(A_, X_) do { float x_ = (X_); _Pragma("unroll") for (int i_ = 0; i_ < 16; ++i_) { const float hi_ = fmaxf(A_[i_], x_); x_ = fminf(A_[i_], x_); A_[i_] = hi_; } } while (0)
; __device__ __forceinline__ float uniq_key(float s, int n) { return __uint_as_float((__float_as_uint(s) & ~0xffu) | (unsigned)(255 - n)); }
; __device__ __forceinline__ void p11_route(Frame& F) {
;     ...
;             { int p = 0;
; #pragma unroll
;               for (int i = 0; i < 16; ++i)
; #pragma unroll
;                   for (int j = 0; j < 16; ++j) if ((i + 1) * (j + 1) <= 16) { INS16(b, uniq_key(v0[i] + v1[j], p)); ++p; } }
	v_min_f32_e32 v233, v225, v233
	v_max_f32_e32 v225, v223, v231
	v_min_f32_e32 v231, v223, v231
	v_max_f32_e32 v223, v224, v232
	v_min_f32_e32 v232, v224, v232
	v_max_f32_e32 v224, v229, v237
	v_min_f32_e32 v237, v229, v237
	v_max_f32_e32 v229, v224, v232
	v_min_f32_e32 v232, v224, v232
	v_max_f32_e32 v224, v223, v225
	v_min_f32_e32 v225, v223, v225
	v_max_f32_e32 v223, v229, v231
	v_min_f32_e32 v231, v229, v231
	v_max_f32_e32 v229, v232, v233
	v_min_f32_e32 v233, v232, v233
	v_max_f32_e32 v232, v230, v222
	v_min_f32_e32 v222, v230, v222
	v_max_f32_e32 v230, v224, v228
	v_min_f32_e32 v228, v224, v228
	v_max_f32_e32 v224, v225, v254
	v_min_f32_e32 v254, v225, v254
	v_max_f32_e32 v225, v223, v227
	v_min_f32_e32 v227, v223, v227
	v_max_f32_e32 v223, v231, v226
	v_min_f32_e32 v226, v231, v226
	v_max_f32_e32 v231, v229, v236
	v_min_f32_e32 v236, v229, v236
	v_max_f32_e32 v229, v233, v234
	v_min_f32_e32 v234, v233, v234
	v_add_f32_e32 v149, v127, v142
	v_and_b32_e32 v149, 0xffffff00, v149
	v_or_b32_e32 v149, 0xef, v149
	v_add_f32_e32 v172, v127, v143
	v_and_b32_e32 v172, 0xffffff00, v172
	v_or_b32_e32 v172, 0xee, v172
	v_add_f32_e32 v173, v127, v144
	v_and_b32_e32 v173, 0xffffff00, v173
	v_or_b32_e32 v173, 0xed, v173
	v_add_f32_e32 v174, v127, v145
	v_and_b32_e32 v174, 0xffffff00, v174
	v_or_b32_e32 v174, 0xec, v174
	v_add_f32_e32 v175, v127, v160
	v_and_b32_e32 v175, 0xffffff00, v175
	v_or_b32_e32 v175, 0xeb, v175
	v_add_f32_e32 v176, v127, v161
	v_and_b32_e32 v176, 0xffffff00, v176
	v_or_b32_e32 v176, 0xea, v176
	v_add_f32_e32 v177, v127, v162
	v_and_b32_e32 v177, 0xffffff00, v177
	v_or_b32_e32 v177, 0xe9, v177
	v_add_f32_e32 v178, v127, v163
	v_and_b32_e32 v178, 0xffffff00, v178
	v_or_b32_e32 v178, 0xe8, v178
	v_add_f32_e32 v179, v128, v142
	v_and_b32_e32 v179, 0xffffff00, v179
	v_or_b32_e32 v179, 0xe7, v179
	v_add_f32_e32 v180, v128, v143
	v_and_b32_e32 v180, 0xffffff00, v180
	v_or_b32_e32 v180, 0xe6, v180
	v_add_f32_e32 v181, v128, v144
	v_and_b32_e32 v181, 0xffffff00, v181
	v_or_b32_e32 v181, 0xe5, v181
	v_add_f32_e32 v182, v128, v145
	v_and_b32_e32 v182, 0xffffff00, v182
	v_or_b32_e32 v182, 0xe4, v182
	v_add_f32_e32 v183, v128, v160
	v_and_b32_e32 v183, 0xffffff00, v183
	v_or_b32_e32 v183, 0xe3, v183
	v_add_f32_e32 v184, v129, v142
	v_and_b32_e32 v184, 0xffffff00, v184
	v_or_b32_e32 v184, 0xe2, v184
	v_add_f32_e32 v185, v129, v143
	v_and_b32_e32 v185, 0xffffff00, v185
	v_or_b32_e32 v185, 0xe1, v185
	v_add_f32_e32 v186, v129, v144
	v_and_b32_e32 v186, 0xffffff00, v186
	v_or_b32_e32 v186, 0xe0, v186
	v_max_f32_e32 v187, v149, v172
	v_min_f32_e32 v172, v149, v172
	v_max_f32_e32 v149, v173, v174
	v_min_f32_e32 v174, v173, v174
	v_max_f32_e32 v173, v187, v149
	v_min_f32_e32 v149, v187, v149
	v_max_f32_e32 v187, v172, v174
	v_min_f32_e32 v174, v172, v174
	v_max_f32_e32 v172, v187, v149
	v_min_f32_e32 v149, v187, v149
	v_max_f32_e32 v187, v175, v176
	v_min_f32_e32 v176, v175, v176
	v_max_f32_e32 v175, v177, v178
	v_min_f32_e32 v178, v177, v178
	v_max_f32_e32 v177, v187, v175
	v_min_f32_e32 v175, v187, v175
	v_max_f32_e32 v187, v176, v178
	v_min_f32_e32 v178, v176, v178
	v_max_f32_e32 v176, v187, v175
	v_min_f32_e32 v175, v187, v175
	v_max_f32_e32 v187, v173, v177
	v_min_f32_e32 v177, v173, v177
	v_max_f32_e32 v173, v149, v175
	v_min_f32_e32 v175, v149, v175
	v_max_f32_e32 v149, v173, v177
	v_min_f32_e32 v177, v173, v177
	v_max_f32_e32 v173, v172, v176
	v_min_f32_e32 v176, v172, v176
	v_max_f32_e32 v172, v174, v178
	v_min_f32_e32 v178, v174, v178
	v_max_f32_e32 v174, v172, v176
	v_min_f32_e32 v176, v172, v176
	v_max_f32_e32 v172, v173, v149
	v_min_f32_e32 v149, v173, v149
	v_max_f32_e32 v173, v174, v177
	v_min_f32_e32 v177, v174, v177
	v_max_f32_e32 v174, v176, v175
	v_min_f32_e32 v175, v176, v175
	v_max_f32_e32 v176, v179, v180
	v_min_f32_e32 v180, v179, v180
	v_max_f32_e32 v179, v181, v182
	v_min_f32_e32 v182, v181, v182
	v_max_f32_e32 v181, v176, v179
	v_min_f32_e32 v179, v176, v179
	v_max_f32_e32 v176, v180, v182
	v_min_f32_e32 v182, v180, v182
	v_max_f32_e32 v180, v176, v179
	v_min_f32_e32 v179, v176, v179
	v_max_f32_e32 v176, v183, v184
	v_min_f32_e32 v184, v183, v184
	v_max_f32_e32 v183, v185, v186
	v_min_f32_e32 v186, v185, v186
	v_max_f32_e32 v185, v176, v183
	v_min_f32_e32 v183, v176, v183
	v_max_f32_e32 v176, v184, v186
	v_min_f32_e32 v186, v184, v186
	v_max_f32_e32 v184, v176, v183
	v_min_f32_e32 v183, v176, v183
	v_max_f32_e32 v176, v181, v185
	v_min_f32_e32 v185, v181, v185
	v_max_f32_e32 v181, v179, v183
	v_min_f32_e32 v183, v179, v183
	v_max_f32_e32 v179, v181, v185
	v_min_f32_e32 v185, v181, v185
	v_max_f32_e32 v181, v180, v184
	v_min_f32_e32 v184, v180, v184
	v_max_f32_e32 v180, v182, v186
	v_min_f32_e32 v186, v182, v186
	v_max_f32_e32 v182, v180, v184
	v_min_f32_e32 v184, v180, v184
	v_max_f32_e32 v180, v181, v179
	v_min_f32_e32 v179, v181, v179
	v_max_f32_e32 v181, v182, v185
	v_min_f32_e32 v185, v182, v185
	v_max_f32_e32 v182, v184, v183
	v_min_f32_e32 v183, v184, v183
	v_max_f32_e32 v184, v187, v176
	v_min_f32_e32 v176, v187, v176
	v_max_f32_e32 v187, v177, v185
	v_min_f32_e32 v185, v177, v185
	v_max_f32_e32 v177, v187, v176
	v_min_f32_e32 v176, v187, v176
	v_max_f32_e32 v187, v149, v179
	v_min_f32_e32 v179, v149, v179
	v_max_f32_e32 v149, v175, v183
	v_min_f32_e32 v183, v175, v183
	v_max_f32_e32 v175, v149, v179
	v_min_f32_e32 v179, v149, v179
	v_max_f32_e32 v149, v187, v177
	v_min_f32_e32 v177, v187, v177
	v_max_f32_e32 v187, v175, v176
	v_min_f32_e32 v176, v175, v176
	v_max_f32_e32 v175, v179, v185
	v_min_f32_e32 v185, v179, v185
	v_max_f32_e32 v179, v172, v180
	v_min_f32_e32 v180, v172, v180
	v_max_f32_e32 v172, v174, v182
; #define INS16(A_, X_) do { float x_ = (X_); _Pragma("unroll") for (int i_ = 0; i_ < 16; ++i_) { const float hi_ = fmaxf(A_[i_], x_); x_ = fminf(A_[i_], x_); A_[i_] = hi_; } } while (0)
; __device__ __forceinline__ float uniq_key(float s, int n) { return __uint_as_float((__float_as_uint(s) & ~0xffu) | (unsigned)(255 - n)); }
; __device__ __forceinline__ void p11_route(Frame& F) {
;     ...
;             { int p = 0;
; #pragma unroll
;               for (int i = 0; i < 16; ++i)
; #pragma unroll
;                   for (int j = 0; j < 16; ++j) if ((i + 1) * (j + 1) <= 16) { INS16(b, uniq_key(v0[i] + v1[j], p)); ++p; } }
	v_min_f32_e32 v182, v174, v182
	v_max_f32_e32 v174, v172, v180
	v_min_f32_e32 v180, v172, v180
	v_max_f32_e32 v172, v173, v181
	v_min_f32_e32 v181, v173, v181
	v_max_f32_e32 v173, v178, v186
	v_min_f32_e32 v186, v178, v186
	v_max_f32_e32 v178, v173, v181
	v_min_f32_e32 v181, v173, v181
	v_max_f32_e32 v173, v172, v174
	v_min_f32_e32 v174, v172, v174
	v_max_f32_e32 v172, v178, v180
	v_min_f32_e32 v180, v178, v180
	v_max_f32_e32 v178, v181, v182
	v_min_f32_e32 v182, v181, v182
	v_max_f32_e32 v181, v179, v149
	v_min_f32_e32 v149, v179, v149
	v_max_f32_e32 v179, v173, v177
	v_min_f32_e32 v177, v173, v177
	v_max_f32_e32 v173, v174, v187
	v_min_f32_e32 v187, v174, v187
	v_max_f32_e32 v174, v172, v176
	v_min_f32_e32 v176, v172, v176
	v_max_f32_e32 v172, v180, v175
	v_min_f32_e32 v175, v180, v175
	v_max_f32_e32 v180, v178, v185
	v_min_f32_e32 v185, v178, v185
	v_max_f32_e32 v178, v182, v183
	v_min_f32_e32 v183, v182, v183
	v_max_f32_e32 v235, v235, v186
	v_max_f32_e32 v232, v232, v183
	v_max_f32_e32 v222, v222, v178
	v_max_f32_e32 v230, v230, v185
	v_max_f32_e32 v228, v228, v180
	v_max_f32_e32 v224, v224, v175
	v_max_f32_e32 v254, v254, v172
	v_max_f32_e32 v225, v225, v176
	v_max_f32_e32 v227, v227, v174
	v_max_f32_e32 v223, v223, v187
	v_max_f32_e32 v226, v226, v173
	v_max_f32_e32 v231, v231, v177
	v_max_f32_e32 v236, v236, v179
	v_max_f32_e32 v229, v229, v149
	v_max_f32_e32 v234, v234, v181
	v_max_f32_e32 v237, v237, v184
	v_max_f32_e32 v233, v235, v227
	v_min_f32_e32 v227, v235, v227
	v_max_f32_e32 v235, v232, v223
	v_min_f32_e32 v223, v232, v223
	v_max_f32_e32 v232, v222, v226
	v_min_f32_e32 v226, v222, v226
	v_max_f32_e32 v222, v230, v231
	v_min_f32_e32 v231, v230, v231
	v_max_f32_e32 v230, v228, v236
	v_min_f32_e32 v236, v228, v236
	v_max_f32_e32 v228, v224, v229
	v_min_f32_e32 v229, v224, v229
	v_max_f32_e32 v224, v254, v234
	v_min_f32_e32 v234, v254, v234
	v_max_f32_e32 v254, v225, v237
	v_min_f32_e32 v237, v225, v237
	v_max_f32_e32 v225, v233, v230
	v_min_f32_e32 v230, v233, v230
	v_max_f32_e32 v233, v235, v228
	v_min_f32_e32 v228, v235, v228
	v_max_f32_e32 v235, v232, v224
	v_min_f32_e32 v224, v232, v224
	v_max_f32_e32 v232, v222, v254
	v_min_f32_e32 v254, v222, v254
	v_max_f32_e32 v222, v227, v236
	v_min_f32_e32 v236, v227, v236
	v_max_f32_e32 v227, v223, v229
	v_min_f32_e32 v229, v223, v229
	v_max_f32_e32 v223, v226, v234
	v_min_f32_e32 v234, v226, v234
	v_max_f32_e32 v226, v231, v237
	v_min_f32_e32 v237, v231, v237
	v_max_f32_e32 v231, v225, v235
	v_min_f32_e32 v235, v225, v235
	v_max_f32_e32 v225, v233, v232
	v_min_f32_e32 v232, v233, v232
	v_max_f32_e32 v233, v230, v224
	v_min_f32_e32 v224, v230, v224
	v_max_f32_e32 v230, v228, v254
	v_min_f32_e32 v254, v228, v254
	v_max_f32_e32 v228, v222, v223
	v_min_f32_e32 v223, v222, v223
	v_max_f32_e32 v222, v227, v226
	v_min_f32_e32 v226, v227, v226
	v_max_f32_e32 v227, v236, v234
	v_min_f32_e32 v234, v236, v234
	v_max_f32_e32 v236, v229, v237
	v_min_f32_e32 v237, v229, v237
	v_max_f32_e32 v229, v231, v225
	v_min_f32_e32 v225, v231, v225
	v_max_f32_e32 v231, v235, v232
	v_min_f32_e32 v232, v235, v232
	v_max_f32_e32 v235, v233, v230
	v_min_f32_e32 v230, v233, v230
	v_max_f32_e32 v233, v224, v254
	v_min_f32_e32 v254, v224, v254
	v_max_f32_e32 v224, v228, v222
	v_min_f32_e32 v222, v228, v222
	v_max_f32_e32 v228, v223, v226
	v_min_f32_e32 v226, v223, v226
	v_max_f32_e32 v223, v227, v236
	v_min_f32_e32 v236, v227, v236
	v_max_f32_e32 v227, v234, v237
	v_min_f32_e32 v237, v234, v237
	v_add_f32_e32 v149, v129, v145
	v_and_b32_e32 v149, 0xffffff00, v149
	v_or_b32_e32 v149, 0xdf, v149
	v_add_f32_e32 v172, v130, v142
	v_and_b32_e32 v172, 0xffffff00, v172
	v_or_b32_e32 v172, 0xde, v172
	v_add_f32_e32 v173, v130, v143
	v_and_b32_e32 v173, 0xffffff00, v173
	v_or_b32_e32 v173, 0xdd, v173
	v_add_f32_e32 v174, v130, v144
	v_and_b32_e32 v174, 0xffffff00, v174
	v_or_b32_e32 v174, 0xdc, v174
	v_add_f32_e32 v175, v131, v142
	v_and_b32_e32 v175, 0xffffff00, v175
	v_or_b32_e32 v175, 0xdb, v175
	v_add_f32_e32 v176, v131, v143
	v_and_b32_e32 v176, 0xffffff00, v176
	v_or_b32_e32 v176, 0xda, v176
	v_add_f32_e32 v177, v132, v142
	v_and_b32_e32 v177, 0xffffff00, v177
	v_or_b32_e32 v177, 0xd9, v177
	v_add_f32_e32 v178, v132, v143
	v_and_b32_e32 v178, 0xffffff00, v178
	v_or_b32_e32 v178, 0xd8, v178
	v_add_f32_e32 v179, v133, v142
	v_and_b32_e32 v179, 0xffffff00, v179
	v_or_b32_e32 v179, 0xd7, v179
	v_add_f32_e32 v180, v133, v143
	v_and_b32_e32 v180, 0xffffff00, v180
	v_or_b32_e32 v180, 0xd6, v180
	v_add_f32_e32 v181, v134, v142
	v_and_b32_e32 v181, 0xffffff00, v181
	v_or_b32_e32 v181, 0xd5, v181
	v_add_f32_e32 v182, v135, v142
	v_and_b32_e32 v182, 0xffffff00, v182
	v_or_b32_e32 v182, 0xd4, v182
	v_add_f32_e32 v183, v136, v142
	v_and_b32_e32 v183, 0xffffff00, v183
	v_or_b32_e32 v183, 0xd3, v183
	v_add_f32_e32 v184, v137, v142
	v_and_b32_e32 v184, 0xffffff00, v184
	v_or_b32_e32 v184, 0xd2, v184
	v_add_f32_e32 v185, v138, v142
	v_and_b32_e32 v185, 0xffffff00, v185
	v_or_b32_e32 v185, 0xd1, v185
	v_add_f32_e32 v186, v139, v142
	v_and_b32_e32 v186, 0xffffff00, v186
	v_or_b32_e32 v186, 0xd0, v186
	v_max_f32_e32 v187, v149, v172
	v_min_f32_e32 v172, v149, v172
	v_max_f32_e32 v149, v173, v174
	v_min_f32_e32 v174, v173, v174
	v_max_f32_e32 v173, v187, v149
	v_min_f32_e32 v149, v187, v149
	v_max_f32_e32 v187, v172, v174
	v_min_f32_e32 v174, v172, v174
	v_max_f32_e32 v172, v187, v149
	v_min_f32_e32 v149, v187, v149
	v_max_f32_e32 v187, v175, v176
	v_min_f32_e32 v176, v175, v176
	v_max_f32_e32 v175, v177, v178
	v_min_f32_e32 v178, v177, v178
	v_max_f32_e32 v177, v187, v175
	v_min_f32_e32 v175, v187, v175
	v_max_f32_e32 v187, v176, v178
; #define INS16(A_, X_) do { float x_ = (X_); _Pragma("unroll") for (int i_ = 0; i_ < 16; ++i_) { const float hi_ = fmaxf(A_[i_], x_); x_ = fminf(A_[i_], x_); A_[i_] = hi_; } } while (0)
; __device__ __forceinline__ float uniq_key(float s, int n) { return __uint_as_float((__float_as_uint(s) & ~0xffu) | (unsigned)(255 - n)); }
; __device__ __forceinline__ void p11_route(Frame& F) {
;     ...
;             { int p = 0;
; #pragma unroll
;               for (int i = 0; i < 16; ++i)
; #pragma unroll
;                   for (int j = 0; j < 16; ++j) if ((i + 1) * (j + 1) <= 16) { INS16(b, uniq_key(v0[i] + v1[j], p)); ++p; } }
	v_min_f32_e32 v178, v176, v178
	v_max_f32_e32 v176, v187, v175
	v_min_f32_e32 v175, v187, v175
	v_max_f32_e32 v187, v173, v177
	v_min_f32_e32 v177, v173, v177
	v_max_f32_e32 v173, v149, v175
	v_min_f32_e32 v175, v149, v175
	v_max_f32_e32 v149, v173, v177
	v_min_f32_e32 v177, v173, v177
	v_max_f32_e32 v173, v172, v176
	v_min_f32_e32 v176, v172, v176
	v_max_f32_e32 v172, v174, v178
	v_min_f32_e32 v178, v174, v178
	v_max_f32_e32 v174, v172, v176
	v_min_f32_e32 v176, v172, v176
	v_max_f32_e32 v172, v173, v149
	v_min_f32_e32 v149, v173, v149
	v_max_f32_e32 v173, v174, v177
	v_min_f32_e32 v177, v174, v177
	v_max_f32_e32 v174, v176, v175
	v_min_f32_e32 v175, v176, v175
	v_max_f32_e32 v176, v179, v180
	v_min_f32_e32 v180, v179, v180
	v_max_f32_e32 v179, v181, v182
	v_min_f32_e32 v182, v181, v182
	v_max_f32_e32 v181, v176, v179
	v_min_f32_e32 v179, v176, v179
	v_max_f32_e32 v176, v180, v182
	v_min_f32_e32 v182, v180, v182
	v_max_f32_e32 v180, v176, v179
	v_min_f32_e32 v179, v176, v179
	v_max_f32_e32 v176, v183, v184
	v_min_f32_e32 v184, v183, v184
	v_max_f32_e32 v183, v185, v186
	v_min_f32_e32 v186, v185, v186
	v_max_f32_e32 v185, v176, v183
	v_min_f32_e32 v183, v176, v183
	v_max_f32_e32 v176, v184, v186
	v_min_f32_e32 v186, v184, v186
	v_max_f32_e32 v184, v176, v183
	v_min_f32_e32 v183, v176, v183
	v_max_f32_e32 v176, v181, v185
	v_min_f32_e32 v185, v181, v185
	v_max_f32_e32 v181, v179, v183
	v_min_f32_e32 v183, v179, v183
	v_max_f32_e32 v179, v181, v185
	v_min_f32_e32 v185, v181, v185
	v_max_f32_e32 v181, v180, v184
	v_min_f32_e32 v184, v180, v184
	v_max_f32_e32 v180, v182, v186
	v_min_f32_e32 v186, v182, v186
	v_max_f32_e32 v182, v180, v184
	v_min_f32_e32 v184, v180, v184
	v_max_f32_e32 v180, v181, v179
	v_min_f32_e32 v179, v181, v179
	v_max_f32_e32 v181, v182, v185
	v_min_f32_e32 v185, v182, v185
	v_max_f32_e32 v182, v184, v183
	v_min_f32_e32 v183, v184, v183
	v_max_f32_e32 v184, v187, v176
	v_min_f32_e32 v176, v187, v176
	v_max_f32_e32 v187, v177, v185
	v_min_f32_e32 v185, v177, v185
	v_max_f32_e32 v177, v187, v176
	v_min_f32_e32 v176, v187, v176
	v_max_f32_e32 v187, v149, v179
	v_min_f32_e32 v179, v149, v179
	v_max_f32_e32 v149, v175, v183
	v_min_f32_e32 v183, v175, v183
	v_max_f32_e32 v175, v149, v179
	v_min_f32_e32 v179, v149, v179
	v_max_f32_e32 v149, v187, v177
	v_min_f32_e32 v177, v187, v177
	v_max_f32_e32 v187, v175, v176
	v_min_f32_e32 v176, v175, v176
	v_max_f32_e32 v175, v179, v185
	v_min_f32_e32 v185, v179, v185
	v_max_f32_e32 v179, v172, v180
	v_min_f32_e32 v180, v172, v180
	v_max_f32_e32 v172, v174, v182
	v_min_f32_e32 v182, v174, v182
	v_max_f32_e32 v174, v172, v180
	v_min_f32_e32 v180, v172, v180
	v_max_f32_e32 v172, v173, v181
	v_min_f32_e32 v181, v173, v181
	v_max_f32_e32 v173, v178, v186
	v_min_f32_e32 v186, v178, v186
	v_max_f32_e32 v178, v173, v181
	v_min_f32_e32 v181, v173, v181
	v_max_f32_e32 v173, v172, v174
	v_min_f32_e32 v174, v172, v174
	v_max_f32_e32 v172, v178, v180
	v_min_f32_e32 v180, v178, v180
	v_max_f32_e32 v178, v181, v182
	v_min_f32_e32 v182, v181, v182
	v_max_f32_e32 v181, v179, v149
	v_min_f32_e32 v149, v179, v149
	v_max_f32_e32 v179, v173, v177
	v_min_f32_e32 v177, v173, v177
	v_max_f32_e32 v173, v174, v187
	v_min_f32_e32 v187, v174, v187
	v_max_f32_e32 v174, v172, v176
	v_min_f32_e32 v176, v172, v176
	v_max_f32_e32 v172, v180, v175
	v_min_f32_e32 v175, v180, v175
	v_max_f32_e32 v180, v178, v185
	v_min_f32_e32 v185, v178, v185
	v_max_f32_e32 v178, v182, v183
	v_min_f32_e32 v183, v182, v183
	v_max_f32_e32 v229, v229, v186
	v_max_f32_e32 v225, v225, v183
	v_max_f32_e32 v231, v231, v178
	v_max_f32_e32 v232, v232, v185
	v_max_f32_e32 v235, v235, v180
	v_max_f32_e32 v230, v230, v175
	v_max_f32_e32 v233, v233, v172
	v_max_f32_e32 v254, v254, v176
	v_max_f32_e32 v224, v224, v174
	v_max_f32_e32 v222, v222, v187
	v_max_f32_e32 v228, v228, v173
	v_max_f32_e32 v226, v226, v177
	v_max_f32_e32 v223, v223, v179
	v_max_f32_e32 v236, v236, v149
	v_max_f32_e32 v227, v227, v181
	v_max_f32_e32 v237, v237, v184
	v_max_f32_e32 v234, v229, v224
	v_min_f32_e32 v224, v229, v224
	v_max_f32_e32 v229, v225, v222
	v_min_f32_e32 v222, v225, v222
	v_max_f32_e32 v225, v231, v228
	v_min_f32_e32 v228, v231, v228
	v_max_f32_e32 v231, v232, v226
	v_min_f32_e32 v226, v232, v226
	v_max_f32_e32 v232, v235, v223
	v_min_f32_e32 v223, v235, v223
	v_max_f32_e32 v235, v230, v236
	v_min_f32_e32 v236, v230, v236
	v_max_f32_e32 v230, v233, v227
	v_min_f32_e32 v227, v233, v227
	v_max_f32_e32 v233, v254, v237
	v_min_f32_e32 v237, v254, v237
	v_max_f32_e32 v254, v234, v232
	v_min_f32_e32 v232, v234, v232
	v_max_f32_e32 v234, v229, v235
	v_min_f32_e32 v235, v229, v235
	v_max_f32_e32 v229, v225, v230
	v_min_f32_e32 v230, v225, v230
	v_max_f32_e32 v225, v231, v233
	v_min_f32_e32 v233, v231, v233
	v_max_f32_e32 v231, v224, v223
	v_min_f32_e32 v223, v224, v223
	v_max_f32_e32 v224, v222, v236
	v_min_f32_e32 v236, v222, v236
	v_max_f32_e32 v222, v228, v227
	v_min_f32_e32 v227, v228, v227
	v_max_f32_e32 v228, v226, v237
	v_min_f32_e32 v237, v226, v237
	v_max_f32_e32 v226, v254, v229
	v_min_f32_e32 v229, v254, v229
	v_max_f32_e32 v254, v234, v225
	v_min_f32_e32 v225, v234, v225
	v_max_f32_e32 v234, v232, v230
	v_min_f32_e32 v230, v232, v230
	v_max_f32_e32 v232, v235, v233
	v_min_f32_e32 v233, v235, v233
	v_max_f32_e32 v235, v231, v222
	v_min_f32_e32 v222, v231, v222
	v_max_f32_e32 v231, v224, v228
	v_min_f32_e32 v228, v224, v228
	v_max_f32_e32 v224, v223, v227
	v_min_f32_e32 v227, v223, v227
	v_max_f32_e32 v223, v236, v237
	v_min_f32_e32 v237, v236, v237
	v_max_f32_e32 v236, v226, v254
	v_min_f32_e32 v254, v226, v254
	v_max_f32_e32 v226, v229, v225
; __device__ __forceinline__ float uniq_key(float s, int n) { return __uint_as_float((__float_as_uint(s) & ~0xffu) | (unsigned)(255 - n)); }
; #define INS16(A_, X_) do { float x_ = (X_); _Pragma("unroll") for (int i_ = 0; i_ < 16; ++i_) { const float hi_ = fmaxf(A_[i_], x_); x_ = fminf(A_[i_], x_); A_[i_] = hi_; } } while (0)
; __device__ __forceinline__ void p11_route(Frame& F) {
;     ...
;             { int p = 0;
; #pragma unroll
;               for (int i = 0; i < 16; ++i)
; #pragma unroll
;                   for (int j = 0; j < 16; ++j) if ((i + 1) * (j + 1) <= 16) { INS16(b, uniq_key(v0[i] + v1[j], p)); ++p; } }
;             const int t = t0 + F.lane; float pv[16]; float den = 0.f; float mx = 0.f;
;             float rsn; { const f32x4* pp = (const f32x4*)((const float*)(F.ws + WS_PSQ) + (size_t)t * 64); float q = 0.f;
; #pragma unroll
;               for (int k = 0; k < 16; ++k) { const f32x4 a4 = pp[k]; q += (a4.x + a4.y) + (a4.z + a4.w); }
	v_min_f32_e32 v225, v229, v225
	v_max_f32_e32 v229, v234, v232
	v_min_f32_e32 v232, v234, v232
	v_max_f32_e32 v234, v230, v233
	v_min_f32_e32 v233, v230, v233
	v_max_f32_e32 v230, v235, v231
	v_min_f32_e32 v231, v235, v231
	v_max_f32_e32 v235, v222, v228
	v_min_f32_e32 v228, v222, v228
	v_max_f32_e32 v222, v224, v223
	v_min_f32_e32 v223, v224, v223
	v_max_f32_e32 v224, v227, v237
	v_min_f32_e32 v237, v227, v237
	v_add_f32_e32 v149, v140, v142
	v_and_b32_e32 v149, 0xffffff00, v149
	v_or_b32_e32 v149, 0xcf, v149
	v_max_f32_e32 v227, v236, v149
	v_min_f32_e32 v236, v236, v149
	v_max_f32_e32 v149, v254, v236
	v_min_f32_e32 v254, v254, v236
	v_max_f32_e32 v236, v226, v254
	v_min_f32_e32 v226, v226, v254
	v_max_f32_e32 v254, v225, v226
	v_min_f32_e32 v225, v225, v226
	v_max_f32_e32 v226, v229, v225
	v_min_f32_e32 v229, v229, v225
	v_max_f32_e32 v225, v232, v229
	v_min_f32_e32 v232, v232, v229
	v_max_f32_e32 v229, v234, v232
	v_min_f32_e32 v234, v234, v232
	v_max_f32_e32 v232, v233, v234
	v_min_f32_e32 v233, v233, v234
	v_max_f32_e32 v234, v230, v233
	v_min_f32_e32 v230, v230, v233
	v_max_f32_e32 v233, v231, v230
	v_min_f32_e32 v231, v231, v230
	v_max_f32_e32 v230, v235, v231
	v_min_f32_e32 v235, v235, v231
	v_max_f32_e32 v231, v228, v235
	v_min_f32_e32 v228, v228, v235
	v_max_f32_e32 v235, v222, v228
	v_min_f32_e32 v222, v222, v228
	v_max_f32_e32 v228, v223, v222
	v_min_f32_e32 v223, v223, v222
	v_max_f32_e32 v222, v224, v223
	v_min_f32_e32 v224, v224, v223
	v_max_f32_e32 v237, v237, v224
	v_add_f32_e32 v172, v141, v142
	v_and_b32_e32 v172, 0xffffff00, v172
	v_or_b32_e32 v172, 0xce, v172
	v_max_f32_e32 v223, v227, v172
	v_min_f32_e32 v227, v227, v172
	v_max_f32_e32 v172, v149, v227
	v_min_f32_e32 v149, v149, v227
	v_max_f32_e32 v227, v236, v149
	v_min_f32_e32 v236, v236, v149
	v_max_f32_e32 v149, v254, v236
	v_min_f32_e32 v254, v254, v236
	v_max_f32_e32 v236, v226, v254
	v_min_f32_e32 v226, v226, v254
	v_max_f32_e32 v254, v225, v226
	v_min_f32_e32 v225, v225, v226
	v_max_f32_e32 v226, v229, v225
	v_min_f32_e32 v229, v229, v225
	v_max_f32_e32 v225, v232, v229
	v_min_f32_e32 v232, v232, v229
	v_max_f32_e32 v229, v234, v232
	v_min_f32_e32 v234, v234, v232
	v_max_f32_e32 v232, v233, v234
	v_min_f32_e32 v233, v233, v234
	v_max_f32_e32 v234, v230, v233
	v_min_f32_e32 v230, v230, v233
	v_max_f32_e32 v233, v231, v230
	v_min_f32_e32 v231, v231, v230
	v_max_f32_e32 v230, v235, v231
	v_min_f32_e32 v235, v235, v231
	v_max_f32_e32 v231, v228, v235
	v_min_f32_e32 v228, v228, v235
	v_max_f32_e32 v235, v222, v228
	v_min_f32_e32 v222, v222, v228
	v_max_f32_e32 v237, v237, v222
	v_mov_b32_e32 v212, v223
	v_mov_b32_e32 v213, v172
	v_mov_b32_e32 v214, v227
	v_mov_b32_e32 v215, v149
	v_mov_b32_e32 v216, v236
	v_mov_b32_e32 v217, v254
	v_mov_b32_e32 v218, v226
	v_mov_b32_e32 v219, v225
	v_mov_b32_e32 v221, v229
	v_mov_b32_e32 v211, v232
	v_mov_b32_e32 v210, v234
	v_mov_b32_e32 v159, v233
	v_mov_b32_e32 v220, v230
	v_add_u32_e32 v130, s18, v1
	v_ashrrev_i32_e32 v131, 31, v130
	v_lshlrev_b64 v[132:133], 8, v[130:131]
	v_lshl_add_u64 v[148:149], s[6:7], 0, v[132:133]
	global_load_dwordx4 v[132:135], v[148:149], off offset:16
	global_load_dwordx4 v[136:139], v[148:149], off
	global_load_dwordx4 v[140:143], v[148:149], off offset:48
	global_load_dwordx4 v[144:147], v[148:149], off offset:32
	global_load_dwordx4 v[160:163], v[148:149], off offset:80
	global_load_dwordx4 v[164:167], v[148:149], off offset:64
	global_load_dwordx4 v[168:171], v[148:149], off offset:112
	global_load_dwordx4 v[172:175], v[148:149], off offset:96
	global_load_dwordx4 v[176:179], v[148:149], off offset:144
	global_load_dwordx4 v[180:183], v[148:149], off offset:128
	global_load_dwordx4 v[126:129], v[148:149], off offset:176
	global_load_dwordx4 v[184:187], v[148:149], off offset:160
	global_load_dwordx4 v[188:191], v[148:149], off offset:208
	global_load_dwordx4 v[192:195], v[148:149], off offset:192
	global_load_dwordx4 v[196:199], v[148:149], off offset:240
	global_load_dwordx4 v[200:203], v[148:149], off offset:224
	s_waitcnt vmcnt(14)
	v_mov_b32_e32 v148, v137
	v_mov_b32_e32 v149, v138
	v_mov_b32_e32 v137, v139
	v_mov_b32_e32 v138, v133
	v_mov_b32_e32 v139, v134
	v_mov_b32_e32 v133, v135
	v_pk_add_f32 v[136:137], v[148:149], v[136:137]
	v_pk_add_f32 v[132:133], v[138:139], v[132:133]
	v_add_f32_e32 v136, v136, v137
	v_pk_add_f32 v[132:133], v[132:133], v[132:133] op_sel:[0,1] op_sel_hi:[1,0]
	v_add_f32_e32 v136, 0, v136
	s_waitcnt vmcnt(13)
	v_mov_b32_e32 v137, v140
	s_waitcnt vmcnt(12)
	v_add_f32_e32 v134, v144, v145
	v_add_f32_e32 v138, v146, v147
	v_mov_b32_e32 v133, v141
	v_mov_b32_e32 v135, v142
	v_mov_b32_e32 v139, v143
	v_pk_add_f32 v[132:133], v[136:137], v[132:133]
	v_pk_add_f32 v[134:135], v[134:135], v[138:139]
	s_waitcnt vmcnt(11)
	v_add_f32_e32 v136, v160, v161
	v_pk_add_f32 v[132:133], v[132:133], v[134:135]
	s_waitcnt vmcnt(10)
	v_mov_b32_e32 v134, v165
	v_mov_b32_e32 v135, v166
	v_mov_b32_e32 v165, v167
	v_pk_add_f32 v[134:135], v[134:135], v[164:165]
	v_pk_add_f32 v[132:133], v[132:133], v[132:133] op_sel:[0,1] op_sel_hi:[1,0]
	v_pk_add_f32 v[134:135], v[134:135], v[134:135] op_sel:[0,1] op_sel_hi:[1,0]
	v_add_f32_e32 v138, v162, v163
	s_waitcnt vmcnt(8)
	v_mov_b32_e32 v133, v172
	v_mov_b32_e32 v135, v173
	v_mov_b32_e32 v137, v174
	v_mov_b32_e32 v139, v175
	v_pk_add_f32 v[132:133], v[132:133], v[134:135]
	v_pk_add_f32 v[134:135], v[136:137], v[138:139]
	s_waitcnt vmcnt(7)
	v_mov_b32_e32 v137, v178
	v_pk_add_f32 v[132:133], v[132:133], v[134:135]
	v_mov_b32_e32 v134, v169
	v_mov_b32_e32 v135, v170
	v_mov_b32_e32 v169, v171
	v_pk_add_f32 v[134:135], v[134:135], v[168:169]
	v_pk_add_f32 v[132:133], v[132:133], v[132:133] op_sel:[0,1] op_sel_hi:[1,0]
	v_pk_add_f32 v[134:135], v[134:135], v[134:135] op_sel:[0,1] op_sel_hi:[1,0]
	s_waitcnt vmcnt(6)
; __device__ __forceinline__ void p11_route(Frame& F) {
;     ...
;             float rsn; { const f32x4* pp = (const f32x4*)((const float*)(F.ws + WS_PSQ) + (size_t)t * 64); float q = 0.f;
; #pragma unroll
;               for (int k = 0; k < 16; ++k) { const f32x4 a4 = pp[k]; q += (a4.x + a4.y) + (a4.z + a4.w); }
;               rsn = 1.0f / sqrtf(q * (1.f / D_) + 1e-6f); }
; #pragma unroll
;             for (int r = 0; r < 16; ++r) { const int p = 255 - (int)(__float_as_uint(b[r]) & 255u); const int ij = ptab[p]; const int ii = ij >> 4, jj = ij & 15;
;                 const float val = r0[ii] + r1[jj]; if (r == 0) mx = val; pv[r] = __expf((val - mx) * rsn); den += pv[r];
;                 PIDX[(size_t)t * 128 + h * PT + r] = __float_as_int(r0[16 + ii]) * PNK + __float_as_int(r1[16 + jj]); }
	v_add_f32_e32 v136, v180, v181
	v_add_f32_e32 v138, v182, v183
	v_mov_b32_e32 v133, v176
	v_mov_b32_e32 v135, v177
	v_mov_b32_e32 v139, v179
	v_pk_add_f32 v[132:133], v[132:133], v[134:135]
	v_pk_add_f32 v[134:135], v[136:137], v[138:139]
	s_waitcnt vmcnt(5)
	v_add_f32_e32 v126, v126, v127
	v_pk_add_f32 v[132:133], v[132:133], v[134:135]
	s_waitcnt vmcnt(4)
	v_mov_b32_e32 v134, v185
	v_mov_b32_e32 v135, v186
	v_mov_b32_e32 v185, v187
	v_pk_add_f32 v[134:135], v[134:135], v[184:185]
	v_pk_add_f32 v[132:133], v[132:133], v[132:133] op_sel:[0,1] op_sel_hi:[1,0]
	v_pk_add_f32 v[134:135], v[134:135], v[134:135] op_sel:[0,1] op_sel_hi:[1,0]
	v_add_f32_e32 v128, v128, v129
	s_waitcnt vmcnt(2)
	v_mov_b32_e32 v133, v192
	v_mov_b32_e32 v135, v193
	v_mov_b32_e32 v127, v194
	v_mov_b32_e32 v129, v195
	v_pk_add_f32 v[132:133], v[132:133], v[134:135]
	v_pk_add_f32 v[126:127], v[126:127], v[128:129]
	v_mov_b32_e32 v128, v189
	v_mov_b32_e32 v129, v190
	v_mov_b32_e32 v189, v191
	v_pk_add_f32 v[126:127], v[132:133], v[126:127]
	v_pk_add_f32 v[128:129], v[128:129], v[188:189]
	v_pk_add_f32 v[126:127], v[126:127], v[126:127] op_sel:[0,1] op_sel_hi:[1,0]
	v_pk_add_f32 v[128:129], v[128:129], v[128:129] op_sel:[0,1] op_sel_hi:[1,0]
	s_waitcnt vmcnt(0)
	v_add_f32_e32 v132, v200, v201
	v_add_f32_e32 v134, v202, v203
	v_mov_b32_e32 v127, v196
	v_mov_b32_e32 v129, v197
	v_mov_b32_e32 v133, v198
	v_mov_b32_e32 v135, v199
	v_pk_add_f32 v[126:127], v[126:127], v[128:129]
	v_pk_add_f32 v[128:129], v[132:133], v[134:135]
	v_xor_b32_e32 v136, -1, v219
	v_pk_add_f32 v[126:127], v[126:127], v[128:129]
	v_add_f32_e32 v126, v126, v127
	v_fmamk_f32 v126, v126, 0x39800000, v157
	v_mul_f32_e32 v127, 0x4f800000, v126
	v_cmp_gt_f32_e32 vcc, s15, v126
	v_cndmask_b32_e32 v126, v126, v127, vcc
	v_sqrt_f32_e32 v127, v126
	v_mov_b32_e32 v146, v231
	v_mov_b32_e32 v147, v235
	v_mov_b32_e32 v148, v237
	v_add_u32_e32 v129, -1, v127
	v_fma_f32 v132, -v129, v127, v126
	v_cmp_ge_f32_e64 s[4:5], 0, v132
	v_add_u32_e32 v132, 1, v127
	v_xor_b32_e32 v134, -1, v217
	v_cndmask_b32_e64 v129, v127, v129, s[4:5]
	v_fma_f32 v127, -v132, v127, v126
	v_cmp_lt_f32_e64 s[4:5], 0, v127
	v_xor_b32_e32 v135, -1, v216
	v_xor_b32_e32 v137, -1, v218
	v_cndmask_b32_e64 v127, v129, v132, s[4:5]
	v_mul_f32_e32 v129, 0x37800000, v127
	v_cndmask_b32_e32 v127, v127, v129, vcc
	v_cmp_class_f32_e32 vcc, v126, v158
	v_and_b32_e32 v136, 0xff, v136
	v_and_b32_e32 v134, 0xff, v134
	v_cndmask_b32_e32 v126, v127, v126, vcc
	v_div_scale_f32 v127, s[4:5], v126, v126, 1.0
	v_rcp_f32_e32 v129, v127
	v_and_b32_e32 v135, 0xff, v135
	v_and_b32_e32 v137, 0xff, v137
	v_lshl_add_u32 v136, v136, 2, s16
	v_fma_f32 v128, -v127, v129, 1.0
	v_fmac_f32_e32 v129, v128, v129
	v_div_scale_f32 v128, vcc, 1.0, v126, 1.0
	v_mul_f32_e32 v132, v128, v129
	v_fma_f32 v133, -v127, v132, v128
	v_fmac_f32_e32 v132, v133, v129
	v_fma_f32 v127, -v127, v132, v128
	v_div_fmas_f32 v127, v127, v129, v132
	v_div_fixup_f32 v167, v127, v126, 1.0
	v_lshlrev_b64 v[126:127], 9, v[130:131]
	v_xor_b32_e32 v131, -1, v212
	v_xor_b32_e32 v132, -1, v215
	v_xor_b32_e32 v130, -1, v213
	v_and_b32_e32 v131, 0xff, v131
	v_xor_b32_e32 v133, -1, v214
	v_and_b32_e32 v132, 0xff, v132
	v_and_b32_e32 v130, 0xff, v130
	v_lshl_add_u32 v131, v131, 2, s16
	v_and_b32_e32 v133, 0xff, v133
	v_lshl_add_u32 v132, v132, 2, s16
	v_lshl_add_u32 v130, v130, 2, s16
	v_lshl_add_u32 v133, v133, 2, s16
	v_lshl_add_u32 v135, v135, 2, s16
	v_lshl_add_u32 v134, v134, 2, s16
	v_lshl_add_u32 v137, v137, 2, s16
	ds_read_b32 v131, v131
	ds_read_b32 v138, v130
	ds_read_b32 v139, v133
	ds_read_b32 v142, v132
	ds_read_b32 v149, v135
	ds_read_b32 v160, v134
	ds_read_b32 v161, v137
	ds_read_b32 v162, v136
	s_waitcnt lgkmcnt(7)
	v_and_b32_e32 v132, 15, v131
	s_waitcnt lgkmcnt(6)
	v_and_b32_e32 v136, 15, v138
	v_ashrrev_i32_e32 v130, 4, v131
	v_lshl_add_u32 v132, v132, 2, v154
	v_ashrrev_i32_e32 v134, 4, v138
	v_lshl_add_u32 v136, v136, 2, v154
	s_waitcnt lgkmcnt(5)
	v_and_b32_e32 v140, 15, v139
	s_waitcnt lgkmcnt(4)
	v_and_b32_e32 v144, 15, v142
	v_lshl_add_u32 v130, v130, 2, v154
	v_add_u32_e32 v132, 0x2000, v132
	v_lshl_add_u32 v134, v134, 2, v154
	v_add_u32_e32 v136, 0x2000, v136
	v_ashrrev_i32_e32 v138, 4, v139
	v_lshl_add_u32 v140, v140, 2, v154
	v_ashrrev_i32_e32 v143, 4, v142
	v_lshl_add_u32 v144, v144, 2, v154
	ds_read2_b32 v[130:131], v130 offset1:16
	ds_read2_b32 v[132:133], v132 offset0:16 offset1:32
	ds_read2_b32 v[134:135], v134 offset1:16
	ds_read2_b32 v[136:137], v136 offset0:16 offset1:32
	v_lshl_add_u32 v138, v138, 2, v154
	v_add_u32_e32 v140, 0x2000, v140
	v_lshl_add_u32 v142, v143, 2, v154
	v_add_u32_e32 v144, 0x2000, v144
	ds_read2_b32 v[138:139], v138 offset1:16
	ds_read2_b32 v[140:141], v140 offset0:16 offset1:32
	ds_read2_b32 v[142:143], v142 offset1:16
	ds_read2_b32 v[144:145], v144 offset0:16 offset1:32
	s_waitcnt lgkmcnt(4)
	v_add_f32_e32 v164, v134, v136
	v_lshl_add_u32 v134, v131, 7, v133
	v_ashrrev_i32_e32 v131, 4, v149
	v_lshl_add_u64 v[128:129], s[8:9], 0, v[126:127]
	v_lshl_add_u32 v135, v135, 7, v137
	s_waitcnt lgkmcnt(0)
	v_lshl_add_u32 v137, v143, 7, v145
	v_lshl_add_u32 v136, v139, 7, v141
	v_and_b32_e32 v133, 15, v149
	v_lshl_add_u32 v131, v131, 2, v154
	global_store_dwordx4 v[128:129], v[134:137], off
	ds_read2_b32 v[136:137], v131 offset1:16
	v_lshl_add_u32 v131, v133, 2, v154
	v_add_u32_e32 v131, 0x2000, v131
	v_add_f32_e32 v165, v138, v140
	ds_read2_b32 v[138:139], v131 offset0:16 offset1:32
	v_ashrrev_i32_e32 v131, 4, v160
	v_and_b32_e32 v133, 15, v160
	v_lshl_add_u32 v131, v131, 2, v154
	ds_read2_b32 v[134:135], v131 offset1:16
	v_lshl_add_u32 v131, v133, 2, v154
	v_add_u32_e32 v131, 0x2000, v131
	ds_read2_b32 v[140:141], v131 offset0:16 offset1:32
	v_ashrrev_i32_e32 v131, 4, v161
	v_and_b32_e32 v133, 15, v161
	v_lshl_add_u32 v131, v131, 2, v154
	v_add_f32_e32 v166, v142, v144
	ds_read2_b32 v[142:143], v131 offset1:16
	v_lshl_add_u32 v131, v133, 2, v154
	v_add_u32_e32 v131, 0x2000, v131
	ds_read2_b32 v[144:145], v131 offset0:16 offset1:32
	v_ashrrev_i32_e32 v131, 4, v162
	v_and_b32_e32 v133, 15, v162
	v_lshl_add_u32 v131, v131, 2, v154
	s_waitcnt lgkmcnt(4)
; __device__ __forceinline__ void p11_route(Frame& F) {
;     ...
;             for (int r = 0; r < 16; ++r) { const int p = 255 - (int)(__float_as_uint(b[r]) & 255u); const int ij = ptab[p]; const int ii = ij >> 4, jj = ij & 15;
;                 const float val = r0[ii] + r1[jj]; if (r == 0) mx = val; pv[r] = __expf((val - mx) * rsn); den += pv[r];
;                 PIDX[(size_t)t * 128 + h * PT + r] = __float_as_int(r0[16 + ii]) * PNK + __float_as_int(r1[16 + jj]); }
	v_add_f32_e32 v168, v136, v138
	s_waitcnt lgkmcnt(2)
	v_add_f32_e32 v169, v134, v140
	v_lshl_add_u32 v134, v137, 7, v139
	ds_read2_b32 v[136:137], v131 offset1:16
	v_lshl_add_u32 v131, v133, 2, v154
	v_add_u32_e32 v131, 0x2000, v131
	ds_read2_b32 v[138:139], v131 offset0:16 offset1:32
	v_xor_b32_e32 v131, -1, v211
	v_xor_b32_e32 v133, -1, v221
	v_lshl_add_u32 v135, v135, 7, v141
	s_waitcnt lgkmcnt(2)
	v_add_f32_e32 v170, v142, v144
	v_and_b32_e32 v131, 0xff, v131
	v_and_b32_e32 v133, 0xff, v133
	v_xor_b32_e32 v140, -1, v159
	v_xor_b32_e32 v141, -1, v210
	v_xor_b32_e32 v142, -1, v146
	v_xor_b32_e32 v144, -1, v220
	v_xor_b32_e32 v146, -1, v148
	v_xor_b32_e32 v147, -1, v147
	v_lshl_add_u32 v133, v133, 2, s16
	v_lshl_add_u32 v131, v131, 2, s16
	v_and_b32_e32 v140, 0xff, v140
	v_and_b32_e32 v141, 0xff, v141
	v_and_b32_e32 v142, 0xff, v142
	v_and_b32_e32 v144, 0xff, v144
	v_and_b32_e32 v146, 0xff, v146
	v_and_b32_e32 v147, 0xff, v147
	v_lshl_add_u32 v141, v141, 2, s16
	v_lshl_add_u32 v140, v140, 2, s16
	v_lshl_add_u32 v144, v144, 2, s16
	v_lshl_add_u32 v142, v142, 2, s16
	v_lshl_add_u32 v147, v147, 2, s16
	v_lshl_add_u32 v146, v146, 2, s16
	ds_read_b32 v133, v133
	ds_read_b32 v131, v131
	ds_read_b32 v148, v141
	ds_read_b32 v149, v140
	ds_read_b32 v159, v144
	ds_read_b32 v160, v142
	ds_read_b32 v171, v147
	ds_read_b32 v172, v146
	s_waitcnt lgkmcnt(7)
	v_ashrrev_i32_e32 v140, 4, v133
	v_and_b32_e32 v133, 15, v133
	v_lshl_add_u32 v133, v133, 2, v154
	v_add_u32_e32 v133, 0x2000, v133
	ds_read2_b32 v[146:147], v133 offset0:16 offset1:32
	s_waitcnt lgkmcnt(7)
	v_ashrrev_i32_e32 v133, 4, v131
	v_and_b32_e32 v131, 15, v131
	v_lshl_add_u32 v131, v131, 2, v154
	v_add_f32_e32 v173, v136, v138
	v_lshl_add_u32 v137, v137, 7, v139
	v_lshl_add_u32 v136, v143, 7, v145
	v_add_u32_e32 v131, 0x2000, v131
	global_store_dwordx4 v[128:129], v[134:137], off offset:16
	v_lshl_add_u32 v133, v133, 2, v154
	ds_read2_b32 v[136:137], v131 offset0:16 offset1:32
	s_waitcnt lgkmcnt(7)
	v_ashrrev_i32_e32 v131, 4, v148
	ds_read2_b32 v[134:135], v133 offset1:16
	v_and_b32_e32 v133, 15, v148
	v_lshl_add_u32 v131, v131, 2, v154
	ds_read2_b32 v[138:139], v131 offset1:16
	v_lshl_add_u32 v131, v133, 2, v154
	v_add_u32_e32 v131, 0x2000, v131
	v_lshl_add_u32 v140, v140, 2, v154
	ds_read2_b32 v[142:143], v131 offset0:16 offset1:32
	s_waitcnt lgkmcnt(9)
	v_ashrrev_i32_e32 v131, 4, v149
	ds_read2_b32 v[140:141], v140 offset1:16
	v_and_b32_e32 v133, 15, v149
	v_lshl_add_u32 v131, v131, 2, v154
	ds_read2_b32 v[144:145], v131 offset1:16
	v_lshl_add_u32 v131, v133, 2, v154
	v_add_u32_e32 v131, 0x2000, v131
	ds_read2_b32 v[148:149], v131 offset0:16 offset1:32
	s_waitcnt lgkmcnt(11)
	v_ashrrev_i32_e32 v131, 4, v159
	v_and_b32_e32 v133, 15, v159
	v_lshl_add_u32 v131, v131, 2, v154
	s_waitcnt lgkmcnt(2)
	v_add_f32_e32 v174, v140, v146
	v_add_f32_e32 v175, v134, v136
	v_lshl_add_u32 v134, v141, 7, v147
	ds_read2_b32 v[140:141], v131 offset1:16
	v_lshl_add_u32 v131, v133, 2, v154
	v_add_u32_e32 v131, 0x2000, v131
	ds_read2_b32 v[146:147], v131 offset0:16 offset1:32
	v_ashrrev_i32_e32 v131, 4, v160
	v_and_b32_e32 v133, 15, v160
	v_lshl_add_u32 v131, v131, 2, v154
	ds_read2_b32 v[160:161], v131 offset1:16
	v_lshl_add_u32 v131, v133, 2, v154
	v_add_u32_e32 v131, 0x2000, v131
	ds_read2_b32 v[162:163], v131 offset0:16 offset1:32
	v_ashrrev_i32_e32 v131, 4, v171
	v_and_b32_e32 v133, 15, v171
	v_lshl_add_u32 v131, v131, 2, v154
	v_add_f32_e32 v176, v138, v142
	v_lshl_add_u32 v136, v139, 7, v143
	ds_read2_b32 v[138:139], v131 offset1:16
	v_lshl_add_u32 v131, v133, 2, v154
	v_add_u32_e32 v131, 0x2000, v131
	ds_read2_b32 v[142:143], v131 offset0:16 offset1:32
	v_ashrrev_i32_e32 v131, 4, v172
	v_lshl_add_u32 v135, v135, 7, v137
	s_waitcnt lgkmcnt(6)
	v_lshl_add_u32 v137, v145, 7, v149
	v_and_b32_e32 v133, 15, v172
	v_lshl_add_u32 v131, v131, 2, v154
	global_store_dwordx4 v[128:129], v[134:137], off offset:32
	ds_read2_b32 v[136:137], v131 offset1:16
	v_lshl_add_u32 v131, v133, 2, v154
	v_add_u32_e32 v131, 0x2000, v131
	v_add_f32_e32 v177, v144, v148
	ds_read2_b32 v[144:145], v131 offset0:16 offset1:32
	s_waitcnt lgkmcnt(6)
	v_add_f32_e32 v159, v140, v146
	v_lshl_add_u32 v134, v141, 7, v147
	s_waitcnt lgkmcnt(1)
; __device__ __forceinline__ void p11_route(Frame& F) {
;     ...
;             for (int r = 0; r < 16; ++r) { const int p = 255 - (int)(__float_as_uint(b[r]) & 255u); const int ij = ptab[p]; const int ii = ij >> 4, jj = ij & 15;
;                 const float val = r0[ii] + r1[jj]; if (r == 0) mx = val; pv[r] = __expf((val - mx) * rsn); den += pv[r];
;                 PIDX[(size_t)t * 128 + h * PT + r] = __float_as_int(r0[16 + ii]) * PNK + __float_as_int(r1[16 + jj]); }
;             const float inv = 1.0f / den;
; #pragma unroll
;             for (int r = 0; r < 16; ++r) PGT[(size_t)t * 128 + h * PT + r] = pv[r] * inv;
	v_mov_b32_e32 v140, v136
	v_mov_b32_e32 v141, v130
	s_waitcnt lgkmcnt(0)
	v_mov_b32_e32 v130, v144
	v_mov_b32_e32 v131, v132
	v_pk_add_f32 v[130:131], v[140:141], v[130:131]
	v_add_f32_e32 v138, v138, v142
	v_sub_f32_e32 v142, v168, v131
	v_mul_f32_e32 v142, v167, v142
	v_mul_f32_e32 v142, 0x3fb8aa3b, v142
	v_exp_f32_e32 v146, v142
	v_sub_f32_e32 v142, v169, v131
	v_mul_f32_e32 v142, v167, v142
	v_mul_f32_e32 v142, 0x3fb8aa3b, v142
	v_exp_f32_e32 v147, v142
	v_sub_f32_e32 v142, v170, v131
	v_mul_f32_e32 v142, v167, v142
	v_mul_f32_e32 v142, 0x3fb8aa3b, v142
	v_exp_f32_e32 v148, v142
	v_sub_f32_e32 v142, v173, v131
	v_mul_f32_e32 v142, v167, v142
	v_mul_f32_e32 v142, 0x3fb8aa3b, v142
	v_exp_f32_e32 v149, v142
	v_sub_f32_e32 v142, v174, v131
	v_mul_f32_e32 v142, v167, v142
	v_sub_f32_e32 v132, v131, v131
	v_sub_f32_e32 v136, v165, v131
	v_mul_f32_e32 v142, 0x3fb8aa3b, v142
	v_add_f32_e32 v178, v160, v162
	v_mul_f32_e32 v132, v132, v167
	v_sub_f32_e32 v133, v164, v131
	v_mul_f32_e32 v136, v167, v136
	v_exp_f32_e32 v160, v142
	v_sub_f32_e32 v142, v175, v131
	v_mul_f32_e32 v132, 0x3fb8aa3b, v132
	v_mul_f32_e32 v133, v167, v133
	v_mul_f32_e32 v136, 0x3fb8aa3b, v136
	v_mul_f32_e32 v142, v167, v142
	v_exp_f32_e32 v132, v132
	v_mul_f32_e32 v133, 0x3fb8aa3b, v133
	v_exp_f32_e32 v140, v136
	v_sub_f32_e32 v136, v166, v131
	v_mul_f32_e32 v142, 0x3fb8aa3b, v142
	v_lshl_add_u32 v135, v161, 7, v163
	v_exp_f32_e32 v133, v133
	v_mul_f32_e32 v136, v167, v136
	v_exp_f32_e32 v161, v142
	v_sub_f32_e32 v142, v176, v131
	v_mul_f32_e32 v136, 0x3fb8aa3b, v136
	v_mul_f32_e32 v142, v167, v142
	v_exp_f32_e32 v141, v136
	v_mul_f32_e32 v142, 0x3fb8aa3b, v142
	v_add_f32_e32 v136, 0, v132
	v_exp_f32_e32 v162, v142
	v_sub_f32_e32 v142, v177, v131
	v_add_f32_e32 v136, v136, v133
	v_mul_f32_e32 v142, v167, v142
	v_add_f32_e32 v136, v136, v140
	v_mul_f32_e32 v142, 0x3fb8aa3b, v142
	v_add_f32_e32 v136, v136, v141
	v_exp_f32_e32 v163, v142
	v_sub_f32_e32 v142, v159, v131
	v_add_f32_e32 v136, v136, v146
	v_mul_f32_e32 v142, v167, v142
	v_add_f32_e32 v136, v136, v147
	v_mul_f32_e32 v142, 0x3fb8aa3b, v142
	v_add_f32_e32 v136, v136, v148
	v_exp_f32_e32 v164, v142
	v_sub_f32_e32 v142, v178, v131
	v_add_f32_e32 v136, v136, v149
	v_mul_f32_e32 v142, v167, v142
	v_sub_f32_e32 v138, v138, v131
	v_add_f32_e32 v136, v136, v160
	v_mul_f32_e32 v142, 0x3fb8aa3b, v142
	v_mul_f32_e32 v138, v167, v138
	v_sub_f32_e32 v130, v130, v131
	v_add_f32_e32 v136, v136, v161
	v_exp_f32_e32 v165, v142
	v_mul_f32_e32 v138, 0x3fb8aa3b, v138
	v_mul_f32_e32 v130, v167, v130
	v_add_f32_e32 v136, v136, v162
	v_exp_f32_e32 v166, v138
	v_mul_f32_e32 v130, 0x3fb8aa3b, v130
	v_add_f32_e32 v136, v136, v163
	v_exp_f32_e32 v167, v130
	v_add_f32_e32 v130, v136, v164
	v_add_f32_e32 v130, v130, v165
	v_add_f32_e32 v130, v130, v166
	v_add_f32_e32 v130, v130, v167
	v_div_scale_f32 v131, s[4:5], v130, v130, 1.0
	v_rcp_f32_e32 v138, v131
	v_lshl_add_u32 v137, v137, 7, v145
	v_lshl_add_u32 v136, v139, 7, v143
	global_store_dwordx4 v[128:129], v[134:137], off offset:48
	v_fma_f32 v128, -v131, v138, 1.0
	v_fmac_f32_e32 v138, v128, v138
	v_div_scale_f32 v128, vcc, 1.0, v130, 1.0
	v_mul_f32_e32 v129, v128, v138
	v_fma_f32 v134, -v131, v129, v128
	v_fmac_f32_e32 v129, v134, v138
	v_fma_f32 v128, -v131, v129, v128
	v_div_fmas_f32 v128, v128, v138, v129
	v_div_fixup_f32 v130, v128, v130, 1.0
	v_lshl_add_u64 v[134:135], s[10:11], 0, v[126:127]
	v_pk_mul_f32 v[126:127], v[132:133], v[130:131] op_sel_hi:[1,0]
	v_pk_mul_f32 v[128:129], v[140:141], v[130:131] op_sel_hi:[1,0]
	global_store_dwordx4 v[134:135], v[126:129], off
	s_nop 1
	v_pk_mul_f32 v[126:127], v[146:147], v[130:131] op_sel_hi:[1,0]
	v_pk_mul_f32 v[128:129], v[148:149], v[130:131] op_sel_hi:[1,0]
	global_store_dwordx4 v[134:135], v[126:129], off offset:16
	s_nop 1
	v_pk_mul_f32 v[126:127], v[160:161], v[130:131] op_sel_hi:[1,0]
	v_pk_mul_f32 v[128:129], v[162:163], v[130:131] op_sel_hi:[1,0]
	global_store_dwordx4 v[134:135], v[126:129], off offset:32
	s_nop 1
	v_pk_mul_f32 v[126:127], v[164:165], v[130:131] op_sel_hi:[1,0]
	v_pk_mul_f32 v[128:129], v[166:167], v[130:131] op_sel_hi:[1,0]
	global_store_dwordx4 v[134:135], v[126:129], off offset:48
	s_branch .LBB0_3213
